# mixer A pass 1: the wait before taking the prefetched Q of the next query block no longer drains the state stores (vmcnt(4))
# baseline (speedup 1.0000x reference)
; __device__ __forceinline__ void mixer_a_phase(const bf16* AQ, const bf16* AK, const bf16* AV  , bf16* O, float* ST, float* ML, const float* rel_bias, LAS unsigned char* lds, int G, int blk, int tid, int lane, int wave) {
;     ...
;         for (int tile = wave; tile < 16; tile += NWAVES) {
;             const int q0 = 512 * a + 32 * tile, tq = q0 + i5;
;             bf16x8 qf[4];
; #pragma unroll
;             for (int d0 = 0; d0 < 4; ++d0) qf[d0] = qn[d0];
;             { const bool more = tile + NWAVES < 16; const bf16* qp = more ? AQ + (tb0 + tq + 32 * NWAVES) * 512 + h * 64 + 8 * hh : AQ + (tb0 + 512 * a + 16 * i5 + wave) * 512 + h * 64 + 8 * hh;
; #pragma unroll
;               for (int d0 = 0; d0 < 4; ++d0) qn[d0] = *(const bf16x8*)(qp + 16 * d0); }
;             f32x16 o0 = {}, o1 = {}; f32x4 lsum = {0.f, 0.f, 0.f, 0.f}; unsigned orw = 0u; float m = M_FAST, l;
;             band_branch_fast(o0, o1, lsum, orw, qf, Kb, 512, Vb, 512, 1, 0, SEQ, q0 - 64, 5, tab, -tq + 64 + TA_OFF + 8 * hh, vst, lane);
;             { const float la = __shfl(lsum[0], i5 & 15), lb = __shfl(lsum[1], i5 & 15); const float lt = (i5 & 16) ? lb : la;
;               l = (hh == 0) ? lt : 0.0f;
;               if (__builtin_expect(__any(((orw & 0xC000C000u) != 0u) || !(lt > 1.0e-30f)), 0)) {
;                   o0 = f32x16{}; o1 = f32x16{}; m = NEGBIG; l = 0.f;
;                   band_branch(o0, o1, m, l, qf, Kb, 512, Vb, 512, 1, 0, SEQ, q0 - 64, 5, tab, -tq + 64 + TA_OFF + 8 * hh, vst, lane, KAPPA_INV); } }
;             band_state_store(o0, o1, m, l, ST + ((tb0 + tq) * 8 + h) * 64, ML + ((tb0 + tq) * 8 + h) * 2, lane);
.LBB0_370:
	s_or_b64 exec, exec, s[34:35]
	s_add_i32 s14, s14, 8
	v_add_u32_e32 v162, 0x100, v162
	s_and_b64 vcc, exec, s[26:27]
	s_cbranch_vccnz .LBB0_381
	s_waitcnt vmcnt(4)
	v_mov_b64_e32 v[52:53], v[74:75]
	v_mov_b64_e32 v[56:57], v[78:79]
	v_mov_b64_e32 v[60:61], v[82:83]
	v_mov_b64_e32 v[64:65], v[86:87]
	v_mov_b64_e32 v[54:55], v[76:77]
	v_mov_b64_e32 v[58:59], v[80:81]
	v_mov_b64_e32 v[62:63], v[84:85]
	v_mov_b64_e32 v[66:67], v[88:89]
	s_branch .LBB0_359
